# MoE prologues: parallel te[] fill + both initial unit tickets drawn by one early atomic (+2) at phase start; m1
# speedup vs baseline: 1.0016x; 1.0016x over previous
; #define LAS __attribute__((address_space(3)))
; __device__ __forceinline__ int moe_build_tiles(const Args& a, LAS unsigned char* lds, int tid) {
;     unsigned* ctl = (unsigned*)(a.ws + WS_CTL);
;     LAS int* tp = (LAS int*)(lds + MISC_OFF + 1024); LAS int* te = (LAS int*)(lds + TE_OFF); LAS unsigned* cn = (LAS unsigned*)(lds + CNT_OFF);
;     if (tid < NEXP) cn[tid] = __hip_atomic_load(ctl + CW_CNT + 64 * tid, __ATOMIC_RELAXED, __HIP_MEMORY_SCOPE_AGENT);
; __global__ void __launch_bounds__(NWAVES * 64, 2) fwd(Args args) {
;     ...
;     if (IN(PH_GATEUP)) {
;         const int ntiles = __builtin_amdgcn_readfirstlane(moe_build_tiles(args, lds, tid));
;         pg8::MoeOrder<true> S; S.init((const bf16*)(ws + WS_U2), (const bf16*)(ws + WS_WGU), ntiles, 4096, lds, ctl + CW_QUEUE + 64 * (bx & 7), bx & 7);
.LBB0_1004:
	s_cmp_gt_i32 s94, 5
	s_cselect_b64 s[0:1], -1, 0
	s_cmp_lt_i32 s95, 6
	s_cselect_b64 s[2:3], -1, 0
	s_or_b64 s[0:1], s[0:1], s[2:3]
	s_and_b64 vcc, exec, s[0:1]
	v_cmp_gt_u32_e64 s[0:1], 32, v0
	s_cbranch_vccnz .LBB0_1303
	v_readlane_b32 s98, v246, 12
	s_nop 1
	s_and_b32 s98, s98, 7
	s_lshl_b32 s98, s98, 8
	s_add_u32 s98, s92, s98
	s_addc_u32 s99, s93, 0
	s_add_u32 s98, s98, 0x10000
	s_addc_u32 s99, s99, 0
	v_cmp_eq_u32_e32 vcc, 0, v0
	s_and_saveexec_b64 s[100:101], vcc
	v_mov_b32_e32 v250, 0
	v_mov_b32_e32 v251, 2
	s_nop 0
	global_atomic_add v247, v250, v251, s[98:99] sc0
	s_or_b64 exec, exec, s[100:101]
	s_and_saveexec_b64 s[2:3], s[0:1]
	s_cbranch_execz .LBB0_1007
	s_waitcnt vmcnt(23) lgkmcnt(0)
	v_lshlrev_b32_e32 v2, 8, v0
	v_mov_b32_e32 v3, 0
	v_lshl_add_u64 v[2:3], s[92:93], 0, v[2:3]
	v_add_co_u32_e32 v2, vcc, 0x8000, v2
	s_nop 1
	v_addc_co_u32_e32 v3, vcc, 0, v3, vcc
	global_load_dword v1, v[2:3], off sc1
	v_lshl_add_u32 v2, v0, 2, 0
	v_add_u32_e32 v2, 0x20500, v2
	s_waitcnt vmcnt(0)
	ds_write_b32 v2, v1

; #define LAS __attribute__((address_space(3)))
; __device__ __forceinline__ int moe_build_tiles(const Args& a, LAS unsigned char* lds, int tid) {
;     ...
;     if (tid == 0) { int s = 0; for (int e = 0; e < NEXP; ++e) { tp[e] = s; s += (int)((cn[e] + 255u) >> 8); } tp[NEXP] = s; }
;     __syncthreads();
;     for (int e = 0; e < NEXP; ++e) { const int lo = tp[e], hi = tp[e + 1]; for (int t = lo + tid; t < hi; t += 512) te[t] = e; }
;     __syncthreads();
;     return tp[NEXP];
; __global__ void __launch_bounds__(NWAVES * 64, 2) fwd(Args args) {
;     ...
;         const int ntiles = __builtin_amdgcn_readfirstlane(moe_build_tiles(args, lds, tid));
;         pg8::MoeOrder<true> S; S.init((const bf16*)(ws + WS_U2), (const bf16*)(ws + WS_WGU), ntiles, 4096, lds, ctl + CW_QUEUE + 64 * (bx & 7), bx & 7);
;         {
;             const LAS int* tp = (const LAS int*)(lds + MISC_OFF + 1024); const LAS unsigned* cn = (const LAS unsigned*)(lds + CNT_OFF); const LAS int* te = (const LAS int*)(lds + TE_OFF);
;             LAS unsigned short* gidx = (LAS unsigned short*)(lds + IDX_OFF); const int* elist = (const int*)(ws + WS_ELIST);
;             const int total = (ntiles - S.mlo < IDX_TILES ? ntiles - S.mlo : IDX_TILES) * 256;
; #pragma unroll 4
;             for (int q = tid; q < total; q += 512) { const int T = S.mlo + (q >> 8), e = te[T], rank = (T - tp[e]) * 256 + (q & 255); gidx[q] = (unsigned short)elist[(size_t)e * NTOK + (rank < (int)cn[e] ? rank : 0)]; }
.LBB0_1009:
	s_or_b64 exec, exec, s[2:3]
	s_add_i32 s12, 0, 0x20400
	v_mov_b32_e32 v1, s12
	s_waitcnt lgkmcnt(0)
	s_barrier
	s_waitcnt vmcnt(23)
	v_mov_b32_e32 v2, -1
	ds_read_b128 v[248:251], v1
	s_waitcnt lgkmcnt(0)
	v_cmp_le_i32_e32 vcc, v248, v0
	s_nop 1
	v_addc_co_u32_e32 v2, vcc, 0, v2, vcc
	v_cmp_le_i32_e32 vcc, v249, v0
	s_nop 1
	v_addc_co_u32_e32 v2, vcc, 0, v2, vcc
	v_cmp_le_i32_e32 vcc, v250, v0
	s_nop 1
	v_addc_co_u32_e32 v2, vcc, 0, v2, vcc
	v_cmp_le_i32_e32 vcc, v251, v0
	s_nop 1
	v_addc_co_u32_e32 v2, vcc, 0, v2, vcc
	ds_read_b128 v[248:251], v1 offset:16
	s_waitcnt lgkmcnt(0)
	v_cmp_le_i32_e32 vcc, v248, v0
	s_nop 1
	v_addc_co_u32_e32 v2, vcc, 0, v2, vcc
	v_cmp_le_i32_e32 vcc, v249, v0
	s_nop 1
	v_addc_co_u32_e32 v2, vcc, 0, v2, vcc
	v_cmp_le_i32_e32 vcc, v250, v0
	s_nop 1
	v_addc_co_u32_e32 v2, vcc, 0, v2, vcc
	v_cmp_le_i32_e32 vcc, v251, v0
	s_nop 1
	v_addc_co_u32_e32 v2, vcc, 0, v2, vcc
	ds_read_b128 v[248:251], v1 offset:32
	s_waitcnt lgkmcnt(0)
	v_cmp_le_i32_e32 vcc, v248, v0
	s_nop 1
	v_addc_co_u32_e32 v2, vcc, 0, v2, vcc
	v_cmp_le_i32_e32 vcc, v249, v0
	s_nop 1
	v_addc_co_u32_e32 v2, vcc, 0, v2, vcc
	v_cmp_le_i32_e32 vcc, v250, v0
	s_nop 1
	v_addc_co_u32_e32 v2, vcc, 0, v2, vcc
	v_cmp_le_i32_e32 vcc, v251, v0
	s_nop 1
	v_addc_co_u32_e32 v2, vcc, 0, v2, vcc
	ds_read_b128 v[248:251], v1 offset:48
	s_waitcnt lgkmcnt(0)
	v_cmp_le_i32_e32 vcc, v248, v0
	s_nop 1
	v_addc_co_u32_e32 v2, vcc, 0, v2, vcc
	v_cmp_le_i32_e32 vcc, v249, v0
	s_nop 1
	v_addc_co_u32_e32 v2, vcc, 0, v2, vcc
	v_cmp_le_i32_e32 vcc, v250, v0
	s_nop 1
	v_addc_co_u32_e32 v2, vcc, 0, v2, vcc
	v_cmp_le_i32_e32 vcc, v251, v0
	s_nop 1
	v_addc_co_u32_e32 v2, vcc, 0, v2, vcc
	ds_read_b128 v[248:251], v1 offset:64
	s_waitcnt lgkmcnt(0)
	v_cmp_le_i32_e32 vcc, v248, v0
	s_nop 1
	v_addc_co_u32_e32 v2, vcc, 0, v2, vcc
	v_cmp_le_i32_e32 vcc, v249, v0
	s_nop 1
	v_addc_co_u32_e32 v2, vcc, 0, v2, vcc
	v_cmp_le_i32_e32 vcc, v250, v0
	s_nop 1
	v_addc_co_u32_e32 v2, vcc, 0, v2, vcc
	v_cmp_le_i32_e32 vcc, v251, v0
	s_nop 1
	v_addc_co_u32_e32 v2, vcc, 0, v2, vcc
	ds_read_b128 v[248:251], v1 offset:80
	s_waitcnt lgkmcnt(0)
	v_cmp_le_i32_e32 vcc, v248, v0
	s_nop 1
	v_addc_co_u32_e32 v2, vcc, 0, v2, vcc
	v_cmp_le_i32_e32 vcc, v249, v0
	s_nop 1
	v_addc_co_u32_e32 v2, vcc, 0, v2, vcc
	v_cmp_le_i32_e32 vcc, v250, v0
	s_nop 1
	v_addc_co_u32_e32 v2, vcc, 0, v2, vcc
	v_cmp_le_i32_e32 vcc, v251, v0
	s_nop 1
	v_addc_co_u32_e32 v2, vcc, 0, v2, vcc
	ds_read_b128 v[248:251], v1 offset:96
	s_waitcnt lgkmcnt(0)
	v_cmp_le_i32_e32 vcc, v248, v0
	s_nop 1
	v_addc_co_u32_e32 v2, vcc, 0, v2, vcc
	v_cmp_le_i32_e32 vcc, v249, v0
	s_nop 1
	v_addc_co_u32_e32 v2, vcc, 0, v2, vcc
	v_cmp_le_i32_e32 vcc, v250, v0
	s_nop 1
	v_addc_co_u32_e32 v2, vcc, 0, v2, vcc
	v_cmp_le_i32_e32 vcc, v251, v0
	s_nop 1
	v_addc_co_u32_e32 v2, vcc, 0, v2, vcc
	ds_read_b128 v[248:251], v1 offset:112
	s_waitcnt lgkmcnt(0)
	v_cmp_le_i32_e32 vcc, v248, v0
	s_nop 1
	v_addc_co_u32_e32 v2, vcc, 0, v2, vcc
	v_cmp_le_i32_e32 vcc, v249, v0
	s_nop 1
	v_addc_co_u32_e32 v2, vcc, 0, v2, vcc
	v_cmp_le_i32_e32 vcc, v250, v0
	s_nop 1
	v_addc_co_u32_e32 v2, vcc, 0, v2, vcc
	v_cmp_le_i32_e32 vcc, v251, v0
	s_nop 1
	v_addc_co_u32_e32 v2, vcc, 0, v2, vcc
	ds_read_b32 v248, v1 offset:128
	s_waitcnt lgkmcnt(0)
	v_cmp_lt_i32_e32 vcc, v0, v248
	s_and_saveexec_b64 s[2:3], vcc
	v_lshlrev_b32_e32 v3, 2, v0
	v_add_u32_e32 v3, 0x21200, v3
	ds_write_b32 v3, v2
	s_or_b64 exec, exec, s[2:3]
	s_add_i32 s2, 0, 0x20480
	v_mov_b32_e32 v1, s2
	s_waitcnt lgkmcnt(0)
	s_barrier
	ds_read_b32 v1, v1
	v_readlane_b32 s2, v246, 12
	s_and_b32 s13, s2, 7
	s_waitcnt lgkmcnt(0)
	v_readfirstlane_b32 s27, v1
	s_lshl_b32 s52, s27, 1
	s_mul_i32 s53, s52, s13
	s_ashr_i32 s2, s53, 31
	s_lshr_b32 s2, s2, 25
	s_add_i32 s2, s53, s2
	s_ashr_i32 s17, s2, 7
	s_lshl_b32 s54, s17, 3
	s_sub_i32 s2, s27, s54
	s_min_i32 s2, s2, 48
	s_lshl_b32 s16, s2, 8
	v_cmp_gt_i32_e32 vcc, s16, v0
	s_and_saveexec_b64 s[2:3], vcc
	s_cbranch_execz .LBB0_1156
	v_not_b32_e32 v2, v0
	s_add_u32 s4, s92, 0x1a800000
	v_add_u32_e32 v3, s16, v2
	s_movk_i32 s6, 0x1ff
	s_addc_u32 s5, s93, 0
	v_and_b32_e32 v4, 0xff, v0
	v_cmp_lt_u32_e32 vcc, s6, v3
	s_mov_b64 s[8:9], -1
	v_mov_b32_e32 v1, v0
	s_and_saveexec_b64 s[6:7], vcc
	s_cbranch_execz .LBB0_1148
	v_lshrrev_b32_e32 v5, 9, v3
	v_add_u32_e32 v2, -1, v5
	v_or_b32_e32 v1, 0x200, v0
	v_lshrrev_b32_e32 v3, 1, v2
	s_mov_b32 s18, 0
	s_waitcnt vmcnt(22)
	v_add_u32_e32 v6, 1, v3
	v_cmp_lt_u32_e32 vcc, 5, v2
	v_mov_b32_e32 v9, 0
	v_mov_b64_e32 v[2:3], v[0:1]
	s_and_saveexec_b64 s[8:9], vcc
	s_cbranch_execz .LBB0_1142
	v_lshl_add_u32 v2, v0, 1, 0
	v_and_b32_e32 v7, -4, v6
	v_add_u32_e32 v8, 0x22000, v2
	s_mov_b64 s[10:11], 0
	s_add_i32 s19, 0, 0x21200
	s_add_i32 s20, 0, 0x20500
	v_mov_b64_e32 v[2:3], v[0:1]

;     __device__ __forceinline__ void prefetch(int i) const { if (threadIdx.x == 0) tick[(base + i) & 3] = (int)__hip_atomic_fetch_add(qctr, 1u, __ATOMIC_RELAXED, __HIP_MEMORY_SCOPE_AGENT); }
; __global__ void __launch_bounds__(NWAVES * 64, 2) fwd(Args args) {
;     ...
;         S.prefetch(0); S.prefetch(1); __syncthreads();
.LBB0_1156:
	s_or_b64 exec, exec, s[2:3]
	s_lshl_b32 s2, s13, 8
	s_add_u32 s2, s92, s2
	s_addc_u32 s3, s93, 0
	s_add_u32 s6, s2, 0x10000
	s_addc_u32 s7, s3, 0
	s_and_saveexec_b64 s[2:3], s[0:1]
	s_cbranch_execz .LBB0_1162
	s_mov_b64 s[8:9], exec
	v_mbcnt_lo_u32_b32 v1, s8, 0
	v_mbcnt_hi_u32_b32 v1, s9, v1
	v_cmp_eq_u32_e32 vcc, 0, v1
	s_and_saveexec_b64 s[4:5], vcc
	s_cbranch_execz .LBB0_1159
	s_bcnt1_i32_b64 s8, s[8:9]
	v_mov_b32_e32 v2, 0
	v_mov_b32_e32 v3, s8
	s_waitcnt vmcnt(0)
	v_mov_b32_e32 v2, v247
.LBB0_1159:
	s_or_b64 exec, exec, s[4:5]
	s_waitcnt vmcnt(0)
	v_readfirstlane_b32 s8, v2
	s_mov_b64 s[4:5], exec
	s_nop 0
	v_add_u32_e32 v1, s8, v1
	s_add_i32 s8, 0, 0x21c00
	v_mov_b32_e32 v2, s8
	ds_write_b32 v2, v1
	v_mbcnt_lo_u32_b32 v1, s4, 0
	v_mbcnt_hi_u32_b32 v1, s5, v1
	v_cmp_eq_u32_e32 vcc, 0, v1
	s_and_saveexec_b64 s[8:9], vcc
	s_cbranch_execz .LBB0_1161
	s_bcnt1_i32_b64 s4, s[4:5]
	v_mov_b32_e32 v2, 0
	v_mov_b32_e32 v3, s4
	v_add_u32_e32 v2, 1, v247

; #define LAS __attribute__((address_space(3)))
; __device__ __forceinline__ int moe_build_tiles(const Args& a, LAS unsigned char* lds, int tid) {
;     unsigned* ctl = (unsigned*)(a.ws + WS_CTL);
;     LAS int* tp = (LAS int*)(lds + MISC_OFF + 1024); LAS int* te = (LAS int*)(lds + TE_OFF); LAS unsigned* cn = (LAS unsigned*)(lds + CNT_OFF);
;     if (tid < NEXP) cn[tid] = __hip_atomic_load(ctl + CW_CNT + 64 * tid, __ATOMIC_RELAXED, __HIP_MEMORY_SCOPE_AGENT);
; __global__ void __launch_bounds__(NWAVES * 64, 2) fwd(Args args) {
;     ...
;     if (IN(PH_DOWN)) {
;         const int ntiles = __builtin_amdgcn_readfirstlane(moe_build_tiles(args, lds, tid));
;         pg8::MoeOrder<false> S; S.init((const bf16*)(ws + WS_ACT), (const bf16*)(ws + WS_WDN), ntiles, DM, lds, ctl + CW_QUEUE + 64 * (8 + (bx & 7)), bx & 7);
.LBB0_1303:
	s_cmp_gt_i32 s94, 6
	s_cselect_b64 s[0:1], -1, 0
	s_cmp_lt_i32 s95, 7
	s_cselect_b64 s[2:3], -1, 0
	s_or_b64 s[0:1], s[0:1], s[2:3]
	s_and_b64 vcc, exec, s[0:1]
	s_cbranch_vccnz .LBB0_1517
	v_readlane_b32 s98, v246, 12
	s_nop 1
	s_and_b32 s98, s98, 7
	s_lshl_b32 s98, s98, 8
	s_add_u32 s98, s92, s98
	s_addc_u32 s99, s93, 0
	s_add_u32 s98, s98, 0x10800
	s_addc_u32 s99, s99, 0
	v_cmp_eq_u32_e32 vcc, 0, v0
	s_and_saveexec_b64 s[100:101], vcc
	v_mov_b32_e32 v250, 0
	v_mov_b32_e32 v251, 2
	s_nop 0
	global_atomic_add v247, v250, v251, s[98:99] sc0
	s_or_b64 exec, exec, s[100:101]
	v_cmp_gt_u32_e32 vcc, 32, v0
	s_and_saveexec_b64 s[0:1], vcc
	s_cbranch_execz .LBB0_1306
	s_waitcnt vmcnt(23) lgkmcnt(0)
	v_lshlrev_b32_e32 v2, 8, v0
	v_mov_b32_e32 v3, 0
	v_lshl_add_u64 v[2:3], s[92:93], 0, v[2:3]
	v_add_co_u32_e32 v2, vcc, 0x8000, v2
	s_nop 1
	v_addc_co_u32_e32 v3, vcc, 0, v3, vcc
	global_load_dword v1, v[2:3], off sc1
	v_lshl_add_u32 v2, v0, 2, 0
	v_add_u32_e32 v2, 0x20500, v2
	s_waitcnt vmcnt(0)
	ds_write_b32 v2, v1

;     __device__ __forceinline__ void prefetch(int i) const { if (threadIdx.x == 0) tick[(base + i) & 3] = (int)__hip_atomic_fetch_add(qctr, 1u, __ATOMIC_RELAXED, __HIP_MEMORY_SCOPE_AGENT); }
; __device__ __forceinline__ int moe_build_tiles(const Args& a, LAS unsigned char* lds, int tid) {
;     ...
;     if (tid == 0) { int s = 0; for (int e = 0; e < NEXP; ++e) { tp[e] = s; s += (int)((cn[e] + 255u) >> 8); } tp[NEXP] = s; }
;     __syncthreads();
;     for (int e = 0; e < NEXP; ++e) { const int lo = tp[e], hi = tp[e + 1]; for (int t = lo + tid; t < hi; t += 512) te[t] = e; }
;     __syncthreads();
;     return tp[NEXP];
; __global__ void __launch_bounds__(NWAVES * 64, 2) fwd(Args args) {
;     ...
;         const int ntiles = __builtin_amdgcn_readfirstlane(moe_build_tiles(args, lds, tid));
;         pg8::MoeOrder<false> S; S.init((const bf16*)(ws + WS_ACT), (const bf16*)(ws + WS_WDN), ntiles, DM, lds, ctl + CW_QUEUE + 64 * (8 + (bx & 7)), bx & 7);
;         S.prefetch(0); S.prefetch(1); __syncthreads();
.LBB0_1308:
	s_or_b64 exec, exec, s[2:3]
	s_add_i32 s2, 0, 0x20400
	v_mov_b32_e32 v1, s2
	s_waitcnt lgkmcnt(0)
	s_barrier
	v_mov_b32_e32 v2, -1
	ds_read_b128 v[248:251], v1
	s_waitcnt lgkmcnt(0)
	v_cmp_le_i32_e32 vcc, v248, v0
	s_nop 1
	v_addc_co_u32_e32 v2, vcc, 0, v2, vcc
	v_cmp_le_i32_e32 vcc, v249, v0
	s_nop 1
	v_addc_co_u32_e32 v2, vcc, 0, v2, vcc
	v_cmp_le_i32_e32 vcc, v250, v0
	s_nop 1
	v_addc_co_u32_e32 v2, vcc, 0, v2, vcc
	v_cmp_le_i32_e32 vcc, v251, v0
	s_nop 1
	v_addc_co_u32_e32 v2, vcc, 0, v2, vcc
	ds_read_b128 v[248:251], v1 offset:16
	s_waitcnt lgkmcnt(0)
	v_cmp_le_i32_e32 vcc, v248, v0
	s_nop 1
	v_addc_co_u32_e32 v2, vcc, 0, v2, vcc
	v_cmp_le_i32_e32 vcc, v249, v0
	s_nop 1
	v_addc_co_u32_e32 v2, vcc, 0, v2, vcc
	v_cmp_le_i32_e32 vcc, v250, v0
	s_nop 1
	v_addc_co_u32_e32 v2, vcc, 0, v2, vcc
	v_cmp_le_i32_e32 vcc, v251, v0
	s_nop 1
	v_addc_co_u32_e32 v2, vcc, 0, v2, vcc
	ds_read_b128 v[248:251], v1 offset:32
	s_waitcnt lgkmcnt(0)
	v_cmp_le_i32_e32 vcc, v248, v0
	s_nop 1
	v_addc_co_u32_e32 v2, vcc, 0, v2, vcc
	v_cmp_le_i32_e32 vcc, v249, v0
	s_nop 1
	v_addc_co_u32_e32 v2, vcc, 0, v2, vcc
	v_cmp_le_i32_e32 vcc, v250, v0
	s_nop 1
	v_addc_co_u32_e32 v2, vcc, 0, v2, vcc
	v_cmp_le_i32_e32 vcc, v251, v0
	s_nop 1
	v_addc_co_u32_e32 v2, vcc, 0, v2, vcc
	ds_read_b128 v[248:251], v1 offset:48
	s_waitcnt lgkmcnt(0)
	v_cmp_le_i32_e32 vcc, v248, v0
	s_nop 1
	v_addc_co_u32_e32 v2, vcc, 0, v2, vcc
	v_cmp_le_i32_e32 vcc, v249, v0
	s_nop 1
	v_addc_co_u32_e32 v2, vcc, 0, v2, vcc
	v_cmp_le_i32_e32 vcc, v250, v0
	s_nop 1
	v_addc_co_u32_e32 v2, vcc, 0, v2, vcc
	v_cmp_le_i32_e32 vcc, v251, v0
	s_nop 1
	v_addc_co_u32_e32 v2, vcc, 0, v2, vcc
	ds_read_b128 v[248:251], v1 offset:64
	s_waitcnt lgkmcnt(0)
	v_cmp_le_i32_e32 vcc, v248, v0
	s_nop 1
	v_addc_co_u32_e32 v2, vcc, 0, v2, vcc
	v_cmp_le_i32_e32 vcc, v249, v0
	s_nop 1
	v_addc_co_u32_e32 v2, vcc, 0, v2, vcc
	v_cmp_le_i32_e32 vcc, v250, v0
	s_nop 1
	v_addc_co_u32_e32 v2, vcc, 0, v2, vcc
	v_cmp_le_i32_e32 vcc, v251, v0
	s_nop 1
	v_addc_co_u32_e32 v2, vcc, 0, v2, vcc
	ds_read_b128 v[248:251], v1 offset:80
	s_waitcnt lgkmcnt(0)
	v_cmp_le_i32_e32 vcc, v248, v0
	s_nop 1
	v_addc_co_u32_e32 v2, vcc, 0, v2, vcc
	v_cmp_le_i32_e32 vcc, v249, v0
	s_nop 1
	v_addc_co_u32_e32 v2, vcc, 0, v2, vcc
	v_cmp_le_i32_e32 vcc, v250, v0
	s_nop 1
	v_addc_co_u32_e32 v2, vcc, 0, v2, vcc
	v_cmp_le_i32_e32 vcc, v251, v0
	s_nop 1
	v_addc_co_u32_e32 v2, vcc, 0, v2, vcc
	ds_read_b128 v[248:251], v1 offset:96
	s_waitcnt lgkmcnt(0)
	v_cmp_le_i32_e32 vcc, v248, v0
	s_nop 1
	v_addc_co_u32_e32 v2, vcc, 0, v2, vcc
	v_cmp_le_i32_e32 vcc, v249, v0
	s_nop 1
	v_addc_co_u32_e32 v2, vcc, 0, v2, vcc
	v_cmp_le_i32_e32 vcc, v250, v0
	s_nop 1
	v_addc_co_u32_e32 v2, vcc, 0, v2, vcc
	v_cmp_le_i32_e32 vcc, v251, v0
	s_nop 1
	v_addc_co_u32_e32 v2, vcc, 0, v2, vcc
	ds_read_b128 v[248:251], v1 offset:112
	s_waitcnt lgkmcnt(0)
	v_cmp_le_i32_e32 vcc, v248, v0
	s_nop 1
	v_addc_co_u32_e32 v2, vcc, 0, v2, vcc
	v_cmp_le_i32_e32 vcc, v249, v0
	s_nop 1
	v_addc_co_u32_e32 v2, vcc, 0, v2, vcc
	v_cmp_le_i32_e32 vcc, v250, v0
	s_nop 1
	v_addc_co_u32_e32 v2, vcc, 0, v2, vcc
	v_cmp_le_i32_e32 vcc, v251, v0
	s_nop 1
	v_addc_co_u32_e32 v2, vcc, 0, v2, vcc
	ds_read_b32 v248, v1 offset:128
	s_waitcnt lgkmcnt(0)
	v_cmp_lt_i32_e32 vcc, v0, v248
	s_and_saveexec_b64 s[2:3], vcc
	v_lshlrev_b32_e32 v3, 2, v0
	v_add_u32_e32 v3, 0x21200, v3
	ds_write_b32 v3, v2
	s_or_b64 exec, exec, s[2:3]
	s_add_i32 s2, 0, 0x20480
	v_mov_b32_e32 v1, s2
	v_readlane_b32 s2, v246, 12
	s_waitcnt lgkmcnt(0)
	s_barrier
	ds_read_b32 v1, v1
	s_and_b32 s12, s2, 7
	s_lshl_b32 s2, s12, 8
	s_add_u32 s2, s92, s2
	s_addc_u32 s3, s93, 0
	s_add_u32 s2, s2, 0x10800
	s_waitcnt lgkmcnt(0)
	v_readfirstlane_b32 s33, v1
	s_addc_u32 s3, s3, 0
	s_and_saveexec_b64 s[4:5], s[0:1]
	s_cbranch_execz .LBB0_1441
	s_mov_b64 s[8:9], exec
	v_mbcnt_lo_u32_b32 v1, s8, 0
	v_mbcnt_hi_u32_b32 v1, s9, v1
	v_cmp_eq_u32_e32 vcc, 0, v1
	s_and_saveexec_b64 s[6:7], vcc
	s_cbranch_execz .LBB0_1438
	s_bcnt1_i32_b64 s8, s[8:9]
	v_mov_b32_e32 v2, 0
	v_mov_b32_e32 v3, s8
	s_waitcnt vmcnt(0)
	v_mov_b32_e32 v2, v247
.LBB0_1438:
	s_or_b64 exec, exec, s[6:7]
	s_waitcnt vmcnt(0)
	v_readfirstlane_b32 s8, v2
	s_mov_b64 s[6:7], exec
	s_nop 0
	v_add_u32_e32 v1, s8, v1
	s_add_i32 s8, 0, 0x21c00
	v_mov_b32_e32 v2, s8
	ds_write_b32 v2, v1
	v_mbcnt_lo_u32_b32 v1, s6, 0
	v_mbcnt_hi_u32_b32 v1, s7, v1
	v_cmp_eq_u32_e32 vcc, 0, v1
	s_and_saveexec_b64 s[8:9], vcc
	s_cbranch_execz .LBB0_1440
	s_bcnt1_i32_b64 s6, s[6:7]
	v_mov_b32_e32 v2, 0
	v_mov_b32_e32 v3, s6
	v_add_u32_e32 v2, 1, v247
